# f2
# speedup vs baseline: 1.0492x; 1.0046x over previous
.LBB6_29:
	ds_bpermute_b32 v33, v165, v38
	s_mov_b32 s10, 0x42800000
	s_mul_i32 s34, s30, 33
	s_mul_hi_i32 s33, s30, 33
	s_add_u32 s2, s34, s6
	s_waitcnt lgkmcnt(0)
	v_add_f32_e32 v33, v38, v33
	v_div_scale_f32 v34, s[4:5], v33, v33, s10
	v_rcp_f32_e32 v35, v34
	s_addc_u32 s3, s33, 0
	s_lshl_b32 s7, s28, 10
	s_add_u32 s4, s26, s7
	v_fma_f32 v36, -v34, v35, 1.0
	v_fmac_f32_e32 v35, v36, v35
	v_div_scale_f32 v36, vcc, s10, v33, s10
	v_mul_f32_e32 v37, v36, v35
	v_fma_f32 v38, -v34, v37, v36
	v_fmac_f32_e32 v37, v38, v35
	v_fma_f32 v34, -v34, v37, v36
	v_div_fmas_f32 v34, v34, v35, v37
	v_div_fixup_f32 v33, v34, v33, s10
	v_mul_f32_e32 v34, v16, v33
	v_mul_f32_e32 v17, v17, v33
	v_mov_b32_e32 v16, 0
	v_cvt_pk_fp8_f32 v16, v34, v17
	v_mul_f32_e32 v20, v20, v33
	v_mul_f32_e32 v21, v21, v33
	v_mov_b32_e32 v17, 0
	v_cvt_pk_fp8_f32 v17, v20, v21
	v_mul_f32_e32 v18, v18, v33
	v_mul_f32_e32 v19, v19, v33
	v_cvt_pk_fp8_f32 v16, v18, v19 op_sel:[0,0,1]
	v_mul_f32_e32 v18, v22, v33
	v_mul_f32_e32 v19, v23, v33
	v_cvt_pk_fp8_f32 v17, v18, v19 op_sel:[0,0,1]
	v_mul_f32_e32 v19, v24, v33
	v_mul_f32_e32 v20, v25, v33
	v_mov_b32_e32 v18, 0
	v_cvt_pk_fp8_f32 v18, v19, v20
	v_mul_f32_e32 v20, v28, v33
	v_mul_f32_e32 v23, v29, v33
	v_mov_b32_e32 v19, 0
	s_addc_u32 s5, s27, 0
	v_cvt_pk_fp8_f32 v19, v20, v23
	ds_bpermute_b32 v20, v165, v32
	v_lshl_add_u64 v[150:151], s[4:5], 0, v[158:159]
	s_lshl_b32 s4, s31, 13
	v_or_b32_e32 v86, s4, v158
	ds_read_b128 v[142:145], v86
	ds_read_b128 v[146:149], v86 offset:1024
	v_mul_f32_e32 v21, v26, v33
	v_mul_f32_e32 v22, v27, v33
	s_waitcnt lgkmcnt(2)
	v_add_f32_e32 v34, v32, v20
	v_cvt_pk_fp8_f32 v18, v21, v22 op_sel:[0,0,1]
	v_mul_f32_e32 v21, v30, v33
	v_mul_f32_e32 v22, v31, v33
	v_div_scale_f32 v35, s[8:9], v34, v34, s10
	v_cvt_pk_fp8_f32 v19, v21, v22 op_sel:[0,0,1]
	v_rcp_f32_e32 v36, v35
	s_lshl_b64 s[2:3], s[2:3], 13
	v_lshl_add_u64 v[84:85], v[150:151], 0, s[2:3]
	global_store_dwordx4 v[84:85], v[16:19], off sc1
	s_add_i32 s2, s4, 0x11000
	s_movk_i32 s5, 0x2000
	v_fma_f32 v16, -v35, v36, 1.0
	v_fmac_f32_e32 v36, v16, v36
	s_waitcnt vmcnt(2) lgkmcnt(1)
	v_mfma_f32_32x32x16_bf16 v[18:33], v[142:145], v[104:107], 0
	v_div_scale_f32 v16, vcc, s10, v34, s10
	v_mul_f32_e32 v17, v16, v36
	v_fma_f32 v37, -v35, v17, v16
	v_fmac_f32_e32 v17, v37, v36
	v_or_b32_e32 v37, s4, v158
	ds_read_b128 v[72:75], v37 offset:2048
	ds_read_b128 v[76:79], v37 offset:3072
	s_waitcnt vmcnt(1) lgkmcnt(2)
	v_mfma_f32_32x32x16_bf16 v[18:33], v[146:149], v[100:103], v[18:33]
	v_fma_f32 v16, -v35, v17, v16
	v_div_fmas_f32 v16, v16, v36, v17
	v_div_fixup_f32 v87, v16, v34, s10
	v_mul_f32_e32 v16, v0, v87
	v_mul_f32_e32 v1, v1, v87
	v_mov_b32_e32 v0, 0
	v_cvt_pk_fp8_f32 v0, v16, v1
	s_waitcnt lgkmcnt(1)
	v_mfma_f32_32x32x16_bf16 v[48:63], v[72:75], v[104:107], 0
	v_add_u32_e32 v1, 0x10800, v86
	ds_read_b128 v[68:71], v1
	ds_read_b128 v[64:67], v1 offset:1024
	v_exp_f32_e32 v1, v18
	v_exp_f32_e32 v16, v19
	v_mul_f32_e32 v2, v2, v87
	v_mul_f32_e32 v3, v3, v87
	v_cvt_pk_fp8_f32 v0, v2, v3 op_sel:[0,0,1]
	v_cvt_pk_bf16_f32 v92, v1, v16
	v_exp_f32_e32 v1, v32
	v_exp_f32_e32 v32, v33
	s_waitcnt lgkmcnt(2)
	v_mfma_f32_32x32x16_bf16 v[48:63], v[76:79], v[100:103], v[48:63]
	v_mul_f32_e32 v2, v4, v87
	v_mul_f32_e32 v3, v5, v87
	v_cvt_pk_bf16_f32 v141, v1, v32
	v_mov_b32_e32 v1, 0
	v_exp_f32_e32 v17, v20
	v_exp_f32_e32 v18, v21
	v_exp_f32_e32 v19, v22
	v_exp_f32_e32 v20, v23
	v_exp_f32_e32 v21, v24
	v_exp_f32_e32 v22, v25
	v_cvt_pk_fp8_f32 v1, v2, v3
	v_mul_f32_e32 v4, v6, v87
	v_mul_f32_e32 v2, v7, v87
	v_or_b32_e32 v3, s2, v158
	v_cvt_pk_bf16_f32 v93, v17, v18
	v_cvt_pk_bf16_f32 v94, v19, v20
	v_cvt_pk_bf16_f32 v95, v21, v22
	ds_read_b128 v[134:137], v37 offset:4096
	ds_read_b128 v[112:115], v3 offset:1024
	v_cvt_pk_fp8_f32 v1, v4, v2 op_sel:[0,0,1]
	v_exp_f32_e32 v3, v48
	v_exp_f32_e32 v4, v49
	v_exp_f32_e32 v34, v26
	v_exp_f32_e32 v35, v27
	v_exp_f32_e32 v36, v28
	v_exp_f32_e32 v38, v29
	v_exp_f32_e32 v39, v30
	v_exp_f32_e32 v40, v31
	s_waitcnt lgkmcnt(3)
	v_mfma_f32_32x32x16_bf16 v[16:31], v[68:71], v[92:95], 0
	v_exp_f32_e32 v7, v52
	v_exp_f32_e32 v52, v57
	v_exp_f32_e32 v57, v62
	v_cvt_pk_bf16_f32 v4, v3, v4
	v_exp_f32_e32 v3, v63
	s_mov_b32 s2, 0x3f803f80
	v_add_u32_e32 v2, s4, v166
	s_mov_b32 s3, s2
	v_cvt_pk_bf16_f32 v138, v34, v35
	v_cvt_pk_bf16_f32 v139, v36, v38
	v_cvt_pk_bf16_f32 v140, v39, v40
	ds_read_b128 v[130:133], v37 offset:5120
	ds_read_b128 v[116:119], v2 offset:2048
	ds_read_b128 v[88:91], v2 offset:4096
	v_cvt_pk_bf16_f32 v155, v57, v3
	ds_read_b128 v[120:123], v86 offset:6144
	ds_read_b128 v[80:83], v2 offset:6144
	v_mul_f32_e32 v3, v8, v87
	v_mul_f32_e32 v8, v9, v87
	v_mov_b32_e32 v2, 0
	v_mov_b64_e32 v[162:163], s[2:3]
	s_waitcnt lgkmcnt(7)
	v_mfma_f32_32x32x16_bf16 v[16:31], v[64:67], v[138:141], v[16:31]
	v_cvt_pk_fp8_f32 v2, v3, v8
	v_exp_f32_e32 v5, v50
	v_exp_f32_e32 v6, v51
	v_exp_f32_e32 v48, v53
	v_exp_f32_e32 v49, v54
	v_exp_f32_e32 v50, v55
	v_mul_f32_e32 v9, v10, v87
	s_waitcnt lgkmcnt(6)
	v_mfma_f32_32x32x16_bf16 v[32:47], v[134:137], v[104:107], 0
	v_mul_f32_e32 v10, v11, v87
	v_cvt_pk_fp8_f32 v2, v9, v10 op_sel:[0,0,1]
	v_cvt_pk_bf16_f32 v5, v5, v6
	v_cvt_pk_bf16_f32 v6, v7, v48
	v_cvt_pk_bf16_f32 v7, v49, v50
	v_mul_f32_e32 v12, v12, v87
	v_mul_f32_e32 v13, v13, v87
	v_mfma_f32_4x4x4_16b_bf16 v[8:11], v[162:163], v[92:93], 0
	v_mov_b32_e32 v3, 0
	s_waitcnt lgkmcnt(3)
	v_mfma_f32_32x32x16_bf16 v[16:31], v[116:119], v[4:7], v[16:31]
	v_cvt_pk_fp8_f32 v3, v12, v13
	v_exp_f32_e32 v51, v56
	v_exp_f32_e32 v53, v58
	v_exp_f32_e32 v54, v59
	v_exp_f32_e32 v55, v60
	v_exp_f32_e32 v56, v61
	v_mul_f32_e32 v14, v14, v87
	v_mfma_f32_4x4x4_16b_bf16 v[8:11], v[162:163], v[94:95], v[8:11]
	v_mul_f32_e32 v12, v15, v87
	v_mfma_f32_32x32x16_bf16 v[32:47], v[130:133], v[100:103], v[32:47]
	v_cvt_pk_fp8_f32 v3, v14, v12 op_sel:[0,0,1]
	v_cvt_pk_bf16_f32 v152, v51, v52
	v_cvt_pk_bf16_f32 v153, v53, v54
	v_cvt_pk_bf16_f32 v154, v55, v56
	ds_read_b128 v[124:127], v86 offset:7168
	v_mov_b32_e32 v128, 0
	s_nop 5
	v_exp_f32_e32 v12, v40
	v_mfma_f32_4x4x4_16b_bf16 v[8:11], v[162:163], v[138:139], v[8:11]
	v_exp_f32_e32 v13, v41
	v_mfma_f32_32x32x16_bf16 v[16:31], v[112:115], v[152:155], v[16:31]
	v_exp_f32_e32 v14, v45
	v_exp_f32_e32 v15, v46
	v_mfma_f32_4x4x4_16b_bf16 v[8:11], v[162:163], v[140:141], v[8:11]
	s_waitcnt lgkmcnt(2)
	v_mfma_f32_32x32x16_bf16 v[48:63], v[120:123], v[104:107], 0
	v_mfma_f32_4x4x4_16b_bf16 v[8:11], v[162:163], v[4:5], v[8:11]
	s_nop 1
	v_mfma_f32_4x4x4_16b_bf16 v[4:7], v[162:163], v[6:7], v[8:11]
	s_nop 1
	v_add_co_u32_e32 v8, vcc, s5, v84
	v_mfma_f32_4x4x4_16b_bf16 v[4:7], v[162:163], v[152:153], v[4:7]
	s_nop 0
	v_addc_co_u32_e32 v9, vcc, 0, v85, vcc
	s_add_i32 s5, s4, 0x11800
	global_store_dwordx4 v[8:9], v[0:3], off sc1
	v_exp_f32_e32 v8, v36
	v_exp_f32_e32 v9, v37
	v_mfma_f32_4x4x4_16b_bf16 v[0:3], v[162:163], v[154:155], v[4:7]
	v_exp_f32_e32 v10, v38
	v_or_b32_e32 v4, s5, v158
	ds_read_b128 v[92:95], v4 offset:1024
	v_exp_f32_e32 v4, v32
	v_exp_f32_e32 v5, v33
	v_exp_f32_e32 v6, v34
	v_exp_f32_e32 v7, v35
	v_exp_f32_e32 v11, v39
	v_cvt_pk_bf16_f32 v4, v4, v5
	s_waitcnt lgkmcnt(1)
	v_mfma_f32_32x32x16_bf16 v[48:63], v[124:127], v[100:103], v[48:63]
	v_cvt_pk_bf16_f32 v5, v6, v7
	v_cvt_pk_bf16_f32 v6, v8, v9
	v_cvt_pk_bf16_f32 v7, v10, v11
	v_exp_f32_e32 v9, v42
	v_exp_f32_e32 v10, v43
	v_exp_f32_e32 v11, v44
	v_exp_f32_e32 v32, v47
	v_mfma_f32_32x32x16_bf16 v[16:31], v[88:91], v[4:7], v[16:31]
	v_cvt_pk_bf16_f32 v8, v12, v13
	v_cvt_pk_bf16_f32 v9, v9, v10
	v_cvt_pk_bf16_f32 v10, v11, v14
	v_cvt_pk_bf16_f32 v11, v15, v32
	s_add_i32 s4, s4, 0x12000
	v_exp_f32_e32 v12, v56
	v_exp_f32_e32 v13, v57
	v_mfma_f32_4x4x4_16b_bf16 v[0:3], v[162:163], v[4:5], v[0:3]
	v_or_b32_e32 v4, s4, v158
	s_waitcnt lgkmcnt(0)
	v_mfma_f32_32x32x16_bf16 v[16:31], v[92:95], v[8:11], v[16:31]
	ds_read_b128 v[84:87], v4 offset:1024
	v_exp_f32_e32 v4, v48
	v_exp_f32_e32 v5, v49
	v_exp_f32_e32 v14, v61
	v_exp_f32_e32 v15, v62
	v_exp_f32_e32 v32, v63
	v_cvt_pk_bf16_f32 v4, v4, v5
	v_mfma_f32_4x4x4_16b_bf16 v[0:3], v[162:163], v[6:7], v[0:3]
	v_exp_f32_e32 v6, v50
	v_exp_f32_e32 v7, v51
	v_mfma_f32_4x4x4_16b_bf16 v[0:3], v[162:163], v[8:9], v[0:3]
	v_exp_f32_e32 v8, v52
	v_exp_f32_e32 v9, v53
	v_mfma_f32_4x4x4_16b_bf16 v[0:3], v[162:163], v[10:11], v[0:3]
	v_exp_f32_e32 v10, v54
	v_exp_f32_e32 v11, v55
	v_cvt_pk_bf16_f32 v5, v6, v7
	v_cvt_pk_bf16_f32 v6, v8, v9
	v_exp_f32_e32 v9, v58
	v_cvt_pk_bf16_f32 v7, v10, v11
	v_exp_f32_e32 v10, v59
	v_exp_f32_e32 v11, v60
	v_mfma_f32_32x32x16_bf16 v[16:31], v[80:83], v[4:7], v[16:31]
	v_cvt_pk_bf16_f32 v8, v12, v13
	v_cvt_pk_bf16_f32 v9, v9, v10
	v_cvt_pk_bf16_f32 v10, v11, v14
	v_cvt_pk_bf16_f32 v11, v15, v32
	s_cmp_eq_u32 s31, 7
	s_cselect_b64 s[4:5], -1, 0
	s_cmp_lg_u32 s31, 7
	v_mfma_f32_4x4x4_16b_bf16 v[0:3], v[162:163], v[4:5], v[0:3]
	s_waitcnt lgkmcnt(0)
	v_mfma_f32_32x32x16_bf16 v[16:31], v[84:87], v[8:11], v[16:31]
	v_mfma_f32_4x4x4_16b_bf16 v[0:3], v[162:163], v[6:7], v[0:3]
	s_nop 1
	v_mfma_f32_4x4x4_16b_bf16 v[0:3], v[162:163], v[8:9], v[0:3]
	s_nop 1
	v_mfma_f32_4x4x4_16b_bf16 v[32:35], v[162:163], v[10:11], v[0:3]
	s_cbranch_scc1 .LBB6_31
	s_nop 0
	v_or_b32_e32 v0, 0x10000, v158
	ds_read_b128 v[0:3], v0
	v_or_b32_e32 v4, 0x10400, v158
	ds_read_b128 v[36:39], v4
	v_mov_b32_e32 v41, 0
	v_mov_b32_e32 v42, v41
	v_mov_b32_e32 v43, v41
	s_waitcnt lgkmcnt(1)
	v_mfma_f32_32x32x16_bf16 v[0:15], v[0:3], v[104:107], 0
	s_waitcnt lgkmcnt(0)
	v_mfma_f32_32x32x16_bf16 v[0:15], v[36:39], v[100:103], v[0:15]
	s_nop 11
	v_exp_f32_e32 v0, v0
	v_exp_f32_e32 v1, v1
	v_mov_b64_e32 v[8:9], s[2:3]
	v_mov_b32_e32 v10, v41
	v_cndmask_b32_e64 v0, 0, v0, s[0:1]
	v_cndmask_b32_e64 v1, 0, v1, s[0:1]
	v_cvt_pk_bf16_f32 v40, v0, v1
	v_or_b32_e32 v0, 0x20c00, v158
	ds_read_b128 v[0:3], v0
	v_mfma_f32_32x32x16_bf16 v[16:31], v[108:111], v[40:43], v[16:31]
	v_mov_b32_e32 v11, v41
	v_mfma_f32_4x4x4_16b_bf16 v[4:7], v[8:9], v[40:41], v[32:35]
	v_mov_b32_e32 v40, v41
	s_nop 0
	v_mfma_f32_4x4x4_16b_bf16 v[32:35], v[8:9], v[10:11], v[4:7]
	s_waitcnt lgkmcnt(0)
	v_mfma_f32_32x32x16_bf16 v[16:31], v[0:3], v[40:43], v[16:31]

.LBB6_37:
	ds_bpermute_b32 v33, v165, v38
	s_mov_b32 s6, 0x42800000
	s_add_u32 s0, s34, s26
	s_addc_u32 s1, s33, 0
	s_lshl_b64 s[0:1], s[0:1], 13
	s_waitcnt lgkmcnt(0)
	v_add_f32_e32 v33, v38, v33
	v_div_scale_f32 v34, s[4:5], v33, v33, s6
	v_rcp_f32_e32 v35, v34
	v_div_scale_f32 v36, vcc, s6, v33, s6
	s_cmp_lt_u32 s29, 64
	v_fma_f32 v37, -v34, v35, 1.0
	v_fmac_f32_e32 v35, v37, v35
	v_mul_f32_e32 v37, v36, v35
	v_fma_f32 v38, -v34, v37, v36
	v_fmac_f32_e32 v37, v38, v35
	v_fma_f32 v34, -v34, v37, v36
	v_div_fmas_f32 v34, v34, v35, v37
	v_div_fixup_f32 v33, v34, v33, s6
	v_mul_f32_e32 v16, v16, v33
	v_mul_f32_e32 v34, v17, v33
	v_mul_f32_e32 v35, v18, v33
	v_mov_b32_e32 v18, 0
	v_mul_f32_e32 v36, v19, v33
	v_cvt_pk_fp8_f32 v18, v16, v34
	v_mul_f32_e32 v16, v20, v33
	v_mul_f32_e32 v20, v21, v33
	v_mov_b32_e32 v19, 0
	v_cvt_pk_fp8_f32 v19, v16, v20
	v_mul_f32_e32 v16, v22, v33
	v_mul_f32_e32 v20, v23, v33
	v_mul_f32_e32 v21, v25, v33
	v_cvt_pk_fp8_f32 v19, v16, v20 op_sel:[0,0,1]
	v_mul_f32_e32 v16, v24, v33
	v_mov_b32_e32 v20, 0
	v_cvt_pk_fp8_f32 v20, v16, v21
	v_mul_f32_e32 v16, v28, v33
	v_mul_f32_e32 v24, v29, v33
	v_mov_b32_e32 v21, 0
	v_cvt_pk_fp8_f32 v21, v16, v24
	ds_bpermute_b32 v16, v165, v32
	v_mul_f32_e32 v22, v26, v33
	v_mul_f32_e32 v23, v27, v33
	v_cvt_pk_fp8_f32 v20, v22, v23 op_sel:[0,0,1]
	v_mul_f32_e32 v22, v30, v33
	s_waitcnt lgkmcnt(0)
	v_add_f32_e32 v16, v32, v16
	v_mul_f32_e32 v23, v31, v33
	v_div_scale_f32 v24, s[4:5], v16, v16, s6
	v_cvt_pk_fp8_f32 v18, v35, v36 op_sel:[0,0,1]
	v_cvt_pk_fp8_f32 v21, v22, v23 op_sel:[0,0,1]
	v_rcp_f32_e32 v25, v24
	v_lshl_add_u64 v[22:23], v[150:151], 0, s[0:1]
	s_movk_i32 s0, 0x2000
	global_store_dwordx4 v[22:23], v[18:21], off sc1
	v_mov_b32_e32 v17, 0
	s_nop 0
	v_fma_f32 v18, -v24, v25, 1.0
	v_fmac_f32_e32 v25, v18, v25
	v_div_scale_f32 v18, vcc, s6, v16, s6
	v_mul_f32_e32 v19, v18, v25
	v_fma_f32 v20, -v24, v19, v18
	v_fmac_f32_e32 v19, v20, v25
	v_fma_f32 v18, -v24, v19, v18
	v_div_fmas_f32 v18, v18, v25, v19
	v_div_fixup_f32 v16, v18, v16, s6
	v_mul_f32_e32 v18, v0, v16
	v_mul_f32_e32 v1, v1, v16
	v_mov_b32_e32 v0, 0
	v_cvt_pk_fp8_f32 v0, v18, v1
	v_mul_f32_e32 v4, v4, v16
	v_mul_f32_e32 v5, v5, v16
	v_mov_b32_e32 v1, 0
	v_cvt_pk_fp8_f32 v1, v4, v5
	v_mul_f32_e32 v2, v2, v16
	v_mul_f32_e32 v3, v3, v16
	v_cvt_pk_fp8_f32 v0, v2, v3 op_sel:[0,0,1]
	v_mul_f32_e32 v2, v6, v16
	v_mul_f32_e32 v3, v7, v16
	v_cvt_pk_fp8_f32 v1, v2, v3 op_sel:[0,0,1]
	v_mul_f32_e32 v3, v8, v16
	v_mul_f32_e32 v4, v9, v16
	v_mov_b32_e32 v2, 0
	v_cvt_pk_fp8_f32 v2, v3, v4
	v_mul_f32_e32 v4, v12, v16
	v_mul_f32_e32 v7, v13, v16
	v_mov_b32_e32 v3, 0
	v_cvt_pk_fp8_f32 v3, v4, v7
	v_mul_f32_e32 v5, v10, v16
	v_mul_f32_e32 v6, v11, v16
	v_cvt_pk_fp8_f32 v2, v5, v6 op_sel:[0,0,1]
	v_mul_f32_e32 v4, v14, v16
	v_mul_f32_e32 v5, v15, v16
	v_cvt_pk_fp8_f32 v3, v4, v5 op_sel:[0,0,1]
	v_add_co_u32_e32 v4, vcc, s0, v22
	s_cselect_b64 s[0:1], -1, 0
	s_nop 0
	v_addc_co_u32_e32 v5, vcc, 0, v23, vcc
	s_and_b64 s[0:1], s[2:3], s[0:1]
	global_store_dwordx4 v[4:5], v[0:3], off sc1
	s_barrier
	s_and_saveexec_b64 s[2:3], s[0:1]
	s_cbranch_execz .LBB6_39
	v_lshl_or_b32 v16, v164, 1, v157
	v_mul_u32_u24_e32 v0, 0x50, v16
	s_movk_i32 s2, 0x50
	v_or_b32_e32 v0, 0x21000, v0
	v_mov_b32_e32 v1, 0x21140
	v_mad_u32_u24 v1, v16, s2, v1
	ds_read_b128 v[8:11], v0
	ds_read_b128 v[12:15], v1
	v_mov_b32_e32 v0, 0x21280
	v_mad_u32_u24 v0, v16, s2, v0
	v_mov_b32_e32 v1, 0x213c0
	v_mad_u32_u24 v1, v16, s2, v1
	ds_read_b128 v[18:21], v0
	ds_read_b128 v[22:25], v1
	v_mov_b32_e32 v0, 0x21500
	v_mad_u32_u24 v0, v16, s2, v0
	v_mov_b32_e32 v1, 0x21640
	v_mad_u32_u24 v1, v16, s2, v1
	ds_read_b128 v[26:29], v0
	ds_read_b128 v[30:33], v1
	v_mov_b32_e32 v0, 0x21780
	v_mad_u32_u24 v0, v16, s2, v0
	v_mov_b32_e32 v1, 0x218c0
	v_mad_u32_u24 v1, v16, s2, v1
	ds_read_b128 v[34:37], v0
	ds_read_b128 v[38:41], v1
	s_mov_b32 s0, 0xff800000
	s_waitcnt lgkmcnt(6)
	v_max3_f32 v0, v8, s0, v12
	s_waitcnt lgkmcnt(4)
	v_max3_f32 v0, v0, v18, v22
	v_mov_b32_e32 v1, 0x21010
	s_waitcnt lgkmcnt(2)
	v_max3_f32 v0, v0, v26, v30
	v_mad_u32_u24 v43, v16, s2, v1
	v_mov_b32_e32 v1, 0x21020
	s_waitcnt lgkmcnt(0)
	v_max3_f32 v42, v0, v34, v38
	v_mad_u32_u24 v44, v16, s2, v1
	v_mov_b32_e32 v1, 0x21030
	v_sub_f32_e32 v0, v8, v42
	v_mad_u32_u24 v81, v16, s2, v1
	v_sub_f32_e32 v1, v12, v42
	v_exp_f32_e32 v0, v0
	v_exp_f32_e32 v1, v1
	v_mov_b32_e32 v2, 0x21040
	v_mov_b32_e32 v12, v9
	v_mad_u32_u24 v83, v16, s2, v2
	v_pk_mul_f32 v[2:3], v[12:13], v[0:1]
	v_mov_b32_e32 v4, 0x21150
	v_add_f32_e32 v2, 0, v2
	v_add_f32_e32 v6, v2, v3
	v_mov_b32_e32 v3, 0x21290
	v_mad_u32_u24 v47, v16, s2, v3
	v_mov_b32_e32 v3, 0x212a0
	v_mad_u32_u24 v48, v16, s2, v3
	v_mov_b32_e32 v3, 0x212b0
	v_sub_f32_e32 v2, v18, v42
	v_mad_u32_u24 v88, v16, s2, v3
	v_sub_f32_e32 v3, v22, v42
	v_mad_u32_u24 v45, v16, s2, v4
	v_mov_b32_e32 v4, 0x21160
	v_exp_f32_e32 v2, v2
	v_exp_f32_e32 v3, v3
	v_mad_u32_u24 v46, v16, s2, v4
	v_mov_b32_e32 v4, 0x21170
	v_mad_u32_u24 v85, v16, s2, v4
	v_mov_b32_e32 v4, 0x21180
	v_mad_u32_u24 v87, v16, s2, v4
	v_mov_b32_e32 v4, 0x212c0
	v_mov_b32_e32 v22, v19
	v_mad_u32_u24 v89, v16, s2, v4
	v_pk_mul_f32 v[4:5], v[22:23], v[2:3]
	v_pk_fma_f32 v[10:11], v[0:1], v[10:11], 0 op_sel_hi:[0,1,0]
	v_add_f32_e32 v4, v6, v4
	v_add_f32_e32 v8, v4, v5
	v_mov_b32_e32 v5, 0x21510
	v_mad_u32_u24 v51, v16, s2, v5
	v_mov_b32_e32 v5, 0x21520
	v_mad_u32_u24 v52, v16, s2, v5
	v_mov_b32_e32 v5, 0x21530
	v_mov_b32_e32 v6, 0x213d0
	v_sub_f32_e32 v4, v26, v42
	v_mad_u32_u24 v92, v16, s2, v5
	v_sub_f32_e32 v5, v30, v42
	v_mad_u32_u24 v49, v16, s2, v6
	v_mov_b32_e32 v6, 0x213e0
	v_exp_f32_e32 v4, v4
	v_exp_f32_e32 v5, v5
	v_mad_u32_u24 v50, v16, s2, v6
	v_mov_b32_e32 v6, 0x213f0
	v_mad_u32_u24 v90, v16, s2, v6
	v_mov_b32_e32 v6, 0x21400
	v_mad_u32_u24 v91, v16, s2, v6
	v_mov_b32_e32 v6, 0x21540
	v_mov_b32_e32 v30, v27
	v_mad_u32_u24 v93, v16, s2, v6
	v_pk_mul_f32 v[6:7], v[30:31], v[4:5]
	v_mov_b32_e32 v80, v1
	v_add_f32_e32 v6, v8, v6
	v_add_f32_e32 v12, v6, v7
	v_mov_b32_e32 v7, 0x21790
	v_mad_u32_u24 v56, v16, s2, v7
	v_mov_b32_e32 v7, 0x217a0
	v_mad_u32_u24 v68, v16, s2, v7
	v_mov_b32_e32 v7, 0x217b0
	v_mov_b32_e32 v8, 0x21650
	v_sub_f32_e32 v6, v34, v42
	v_mad_u32_u24 v96, v16, s2, v7
	v_sub_f32_e32 v7, v38, v42
	v_mad_u32_u24 v53, v16, s2, v8
	v_mov_b32_e32 v8, 0x21660
	v_exp_f32_e32 v6, v6
	v_exp_f32_e32 v7, v7
	v_mad_u32_u24 v64, v16, s2, v8
	v_mov_b32_e32 v8, 0x21670
	v_mad_u32_u24 v94, v16, s2, v8
	v_mov_b32_e32 v8, 0x21680
	v_mad_u32_u24 v95, v16, s2, v8
	v_mov_b32_e32 v8, 0x217c0
	v_mov_b32_e32 v38, v35
	v_mad_u32_u24 v97, v16, s2, v8
	v_pk_mul_f32 v[8:9], v[38:39], v[6:7]
	v_pk_fma_f32 v[10:11], v[80:81], v[14:15], v[10:11] op_sel_hi:[0,1,1]
	v_add_f32_e32 v8, v12, v8
	v_add_f32_e32 v8, v8, v9
	v_div_scale_f32 v9, s[0:1], v8, v8, 1.0
	v_mov_b32_e32 v12, 0x218d0
	v_rcp_f32_e32 v13, v9
	v_mad_u32_u24 v60, v16, s2, v12
	v_mov_b32_e32 v12, 0x218e0
	v_mad_u32_u24 v72, v16, s2, v12
	v_mov_b32_e32 v12, 0x218f0
	v_mad_u32_u24 v98, v16, s2, v12
	v_mov_b32_e32 v12, 0x21900
	v_mad_u32_u24 v99, v16, s2, v12
	v_fma_f32 v12, -v9, v13, 1.0
	v_fmac_f32_e32 v13, v12, v13
	v_div_scale_f32 v12, vcc, 1.0, v8, 1.0
	v_pk_fma_f32 v[10:11], v[2:3], v[20:21], v[10:11] op_sel_hi:[0,1,1]
	v_mov_b32_e32 v82, v3
	v_mul_f32_e32 v16, v12, v13
	v_pk_fma_f32 v[10:11], v[82:83], v[24:25], v[10:11] op_sel_hi:[0,1,1]
	v_fma_f32 v18, -v9, v16, v12
	s_mul_i32 s0, s30, 0x108
	v_pk_fma_f32 v[10:11], v[4:5], v[28:29], v[10:11] op_sel_hi:[0,1,1]
	v_mov_b32_e32 v84, v5
	v_fmac_f32_e32 v16, v18, v13
	s_mul_hi_i32 s1, s30, 0x108
	s_or_b32 s0, s0, s28
	v_pk_fma_f32 v[10:11], v[84:85], v[32:33], v[10:11] op_sel_hi:[0,1,1]
	v_fma_f32 v9, -v9, v16, v12
	s_lshl_b64 s[0:1], s[0:1], 11
	v_pk_fma_f32 v[10:11], v[6:7], v[36:37], v[10:11] op_sel_hi:[0,1,1]
	v_mov_b32_e32 v86, v7
	v_div_fmas_f32 v9, v9, v13, v16
	s_add_u32 s0, s24, s0
	v_pk_fma_f32 v[14:15], v[86:87], v[40:41], v[10:11] op_sel_hi:[0,1,1]
	ds_read_b128 v[10:13], v43
	s_addc_u32 s1, s25, s1
	v_lshlrev_b32_e32 v16, 1, v156
	v_lshl_add_u64 v[76:77], s[0:1], 0, v[16:17]
	ds_read_b128 v[16:19], v45
	ds_read_b128 v[20:23], v44
	ds_read_b128 v[24:27], v47
	ds_read_b128 v[28:31], v46
	ds_read_b128 v[32:35], v49
	ds_read_b128 v[36:39], v48
	s_waitcnt lgkmcnt(6)
	v_pk_fma_f32 v[10:11], v[0:1], v[10:11], 0 op_sel_hi:[0,1,0]
	ds_read_b128 v[40:43], v51
	ds_read_b128 v[44:47], v50
	s_waitcnt lgkmcnt(7)
	v_pk_fma_f32 v[10:11], v[80:81], v[16:17], v[10:11] op_sel_hi:[0,1,1]
	ds_read_b128 v[48:51], v53
	ds_read_b128 v[52:55], v52
	s_waitcnt lgkmcnt(7)
	v_pk_fma_f32 v[10:11], v[2:3], v[24:25], v[10:11] op_sel_hi:[0,1,1]
	s_waitcnt lgkmcnt(5)
	v_pk_fma_f32 v[10:11], v[82:83], v[32:33], v[10:11] op_sel_hi:[0,1,1]
	ds_read_b128 v[56:59], v56
	ds_read_b128 v[60:63], v60
	ds_read_b128 v[64:67], v64
	s_waitcnt lgkmcnt(6)
	v_pk_fma_f32 v[10:11], v[4:5], v[40:41], v[10:11] op_sel_hi:[0,1,1]
	s_waitcnt lgkmcnt(4)
	v_pk_fma_f32 v[10:11], v[84:85], v[48:49], v[10:11] op_sel_hi:[0,1,1]
	s_waitcnt lgkmcnt(2)
	v_pk_fma_f32 v[10:11], v[6:7], v[56:57], v[10:11] op_sel_hi:[0,1,1]
	v_div_fixup_f32 v8, v9, v8, 1.0
	s_waitcnt lgkmcnt(1)
	v_pk_fma_f32 v[10:11], v[86:87], v[60:61], v[10:11] op_sel_hi:[0,1,1]
	v_pk_mul_f32 v[14:15], v[8:9], v[14:15] op_sel_hi:[0,1]
	v_pk_mul_f32 v[10:11], v[8:9], v[10:11] op_sel_hi:[0,1]
	v_cvt_pk_bf16_f32 v14, v14, v15
	v_cvt_pk_bf16_f32 v15, v10, v11
	v_pk_fma_f32 v[10:11], v[0:1], v[12:13], 0 op_sel_hi:[0,1,0]
	v_pk_fma_f32 v[10:11], v[80:81], v[18:19], v[10:11] op_sel_hi:[0,1,1]
	v_pk_fma_f32 v[10:11], v[2:3], v[26:27], v[10:11] op_sel_hi:[0,1,1]
	v_pk_fma_f32 v[10:11], v[82:83], v[34:35], v[10:11] op_sel_hi:[0,1,1]
	v_pk_fma_f32 v[10:11], v[4:5], v[42:43], v[10:11] op_sel_hi:[0,1,1]
	v_pk_fma_f32 v[10:11], v[84:85], v[50:51], v[10:11] op_sel_hi:[0,1,1]
	v_pk_fma_f32 v[10:11], v[6:7], v[58:59], v[10:11] op_sel_hi:[0,1,1]
	v_pk_fma_f32 v[10:11], v[86:87], v[62:63], v[10:11] op_sel_hi:[0,1,1]
	v_pk_mul_f32 v[10:11], v[8:9], v[10:11] op_sel_hi:[0,1]
	v_cvt_pk_bf16_f32 v16, v10, v11
	v_pk_fma_f32 v[10:11], v[0:1], v[20:21], 0 op_sel_hi:[0,1,0]
	ds_read_b128 v[68:71], v68
	ds_read_b128 v[72:75], v72
	v_pk_fma_f32 v[10:11], v[80:81], v[28:29], v[10:11] op_sel_hi:[0,1,1]
	v_pk_fma_f32 v[10:11], v[2:3], v[36:37], v[10:11] op_sel_hi:[0,1,1]
	v_pk_fma_f32 v[10:11], v[82:83], v[44:45], v[10:11] op_sel_hi:[0,1,1]
	v_pk_fma_f32 v[10:11], v[4:5], v[52:53], v[10:11] op_sel_hi:[0,1,1]
	s_waitcnt lgkmcnt(2)
	v_pk_fma_f32 v[10:11], v[84:85], v[64:65], v[10:11] op_sel_hi:[0,1,1]
	s_waitcnt lgkmcnt(1)
	v_pk_fma_f32 v[10:11], v[6:7], v[68:69], v[10:11] op_sel_hi:[0,1,1]
	s_mov_b64 s[0:1], 0x80000
	s_waitcnt lgkmcnt(0)
	v_pk_fma_f32 v[10:11], v[86:87], v[72:73], v[10:11] op_sel_hi:[0,1,1]
	v_lshl_add_u64 v[78:79], v[76:77], 0, s[0:1]
	v_pk_mul_f32 v[10:11], v[8:9], v[10:11] op_sel_hi:[0,1]
	s_mov_b32 s0, 0x80000
	v_cvt_pk_bf16_f32 v17, v10, v11
	v_add_co_u32_e32 v10, vcc, s0, v76
	s_nop 1
	v_addc_co_u32_e32 v11, vcc, 0, v77, vcc
	global_store_dwordx4 v[10:11], v[14:17], off
	v_pk_fma_f32 v[10:11], v[0:1], v[22:23], 0 op_sel_hi:[0,1,0]
	v_pk_fma_f32 v[10:11], v[80:81], v[30:31], v[10:11] op_sel_hi:[0,1,1]
	v_pk_fma_f32 v[10:11], v[2:3], v[38:39], v[10:11] op_sel_hi:[0,1,1]
	v_pk_fma_f32 v[10:11], v[82:83], v[46:47], v[10:11] op_sel_hi:[0,1,1]
	v_pk_fma_f32 v[10:11], v[4:5], v[54:55], v[10:11] op_sel_hi:[0,1,1]
	v_pk_fma_f32 v[10:11], v[84:85], v[66:67], v[10:11] op_sel_hi:[0,1,1]
	v_pk_fma_f32 v[10:11], v[6:7], v[70:71], v[10:11] op_sel_hi:[0,1,1]
	v_pk_fma_f32 v[14:15], v[86:87], v[74:75], v[10:11] op_sel_hi:[0,1,1]
	ds_read_b128 v[10:13], v81
	ds_read_b128 v[16:19], v85
	ds_read_b64 v[44:45], v83
	ds_read_b128 v[20:23], v88
	ds_read_b64 v[46:47], v87
	ds_read_b128 v[24:27], v90
	ds_read_b64 v[48:49], v89
	v_pk_mul_f32 v[14:15], v[8:9], v[14:15] op_sel_hi:[0,1]
	s_waitcnt lgkmcnt(6)
	v_pk_fma_f32 v[10:11], v[0:1], v[10:11], 0 op_sel_hi:[0,1,0]
	s_waitcnt lgkmcnt(5)
	v_pk_fma_f32 v[10:11], v[80:81], v[16:17], v[10:11] op_sel_hi:[0,1,1]
	s_waitcnt lgkmcnt(3)
	v_pk_fma_f32 v[10:11], v[2:3], v[20:21], v[10:11] op_sel_hi:[0,1,1]
	ds_read_b128 v[28:31], v92
	ds_read_b64 v[20:21], v91
	s_waitcnt lgkmcnt(3)
	v_pk_fma_f32 v[10:11], v[82:83], v[24:25], v[10:11] op_sel_hi:[0,1,1]
	ds_read_b128 v[32:35], v94
	ds_read_b64 v[24:25], v93
	v_cvt_pk_bf16_f32 v14, v14, v15
	s_waitcnt lgkmcnt(3)
	v_pk_fma_f32 v[10:11], v[4:5], v[28:29], v[10:11] op_sel_hi:[0,1,1]
	ds_read_b128 v[36:39], v96
	ds_read_b128 v[40:43], v98
	ds_read_b64 v[28:29], v95
	s_waitcnt lgkmcnt(4)
	v_pk_fma_f32 v[10:11], v[84:85], v[32:33], v[10:11] op_sel_hi:[0,1,1]
	ds_read_b64 v[32:33], v97
	s_waitcnt lgkmcnt(3)
	v_pk_fma_f32 v[10:11], v[6:7], v[36:37], v[10:11] op_sel_hi:[0,1,1]
	s_waitcnt lgkmcnt(2)
	v_pk_fma_f32 v[10:11], v[86:87], v[40:41], v[10:11] op_sel_hi:[0,1,1]
	v_pk_mul_f32 v[10:11], v[8:9], v[10:11] op_sel_hi:[0,1]
	v_cvt_pk_bf16_f32 v15, v10, v11
	v_pk_fma_f32 v[10:11], v[0:1], v[12:13], 0 op_sel_hi:[0,1,0]
	v_pk_fma_f32 v[0:1], v[0:1], v[44:45], 0 op_sel_hi:[0,1,0]
	v_pk_fma_f32 v[10:11], v[80:81], v[18:19], v[10:11] op_sel_hi:[0,1,1]
	v_pk_fma_f32 v[0:1], v[80:81], v[46:47], v[0:1] op_sel_hi:[0,1,1]
	ds_read_b64 v[36:37], v99
	v_pk_fma_f32 v[10:11], v[2:3], v[22:23], v[10:11] op_sel_hi:[0,1,1]
	v_pk_fma_f32 v[0:1], v[2:3], v[48:49], v[0:1] op_sel_hi:[0,1,1]
	v_pk_fma_f32 v[10:11], v[82:83], v[26:27], v[10:11] op_sel_hi:[0,1,1]
	v_pk_fma_f32 v[0:1], v[82:83], v[20:21], v[0:1] op_sel_hi:[0,1,1]
	v_pk_fma_f32 v[10:11], v[4:5], v[30:31], v[10:11] op_sel_hi:[0,1,1]
	v_pk_fma_f32 v[0:1], v[4:5], v[24:25], v[0:1] op_sel_hi:[0,1,1]
	v_pk_fma_f32 v[10:11], v[84:85], v[34:35], v[10:11] op_sel_hi:[0,1,1]
	s_waitcnt lgkmcnt(2)
	v_pk_fma_f32 v[0:1], v[84:85], v[28:29], v[0:1] op_sel_hi:[0,1,1]
	v_pk_fma_f32 v[10:11], v[6:7], v[38:39], v[10:11] op_sel_hi:[0,1,1]
	s_waitcnt lgkmcnt(1)
	v_pk_fma_f32 v[0:1], v[6:7], v[32:33], v[0:1] op_sel_hi:[0,1,1]
	v_pk_fma_f32 v[10:11], v[86:87], v[42:43], v[10:11] op_sel_hi:[0,1,1]
	s_waitcnt lgkmcnt(0)
	v_pk_fma_f32 v[0:1], v[86:87], v[36:37], v[0:1] op_sel_hi:[0,1,1]
	v_pk_mul_f32 v[10:11], v[8:9], v[10:11] op_sel_hi:[0,1]
	v_pk_mul_f32 v[0:1], v[8:9], v[0:1] op_sel_hi:[0,1]
	v_cvt_pk_bf16_f32 v16, v10, v11
	v_cvt_pk_bf16_f32 v17, v0, v1
	global_store_dwordx4 v[78:79], v[14:17], off offset:1024
